# v8 + PLE-gate GEMM tiles rebalanced into the idle tails of the MoE gate|up and down phases (each tile still computed once per layer)
# speedup vs baseline: 1.0348x; 1.0009x over previous
.LBB0_721:
	s_mov_b32 s4, 0
	s_nop 0
	v_writelane_b32 v255, s4, 42
	s_cmpk_lt_i32 s92, 0x400
	s_cselect_b64 s[4:5], -1, 0
	s_ashr_i32 s83, s92, 31
	v_writelane_b32 v253, s4, 11
	s_lshr_b32 s3, s83, 29
	s_mov_b32 s35, 0
	v_writelane_b32 v253, s5, 12
	s_add_i32 s4, s92, s3
	s_ashr_i32 s3, s4, 3
	s_and_b32 s4, s4, -8
	s_sub_i32 s4, s92, s4
	s_lshl_b32 s5, s4, 7
	s_cmpk_lt_i32 s92, 0x700
	s_cselect_b64 s[6:7], -1, 0
	v_writelane_b32 v253, s6, 13
	v_mov_b32_e32 v65, 0
	s_mov_b64 s[88:89], 0x80
	v_writelane_b32 v253, s7, 14
	s_mov_b32 s95, 0x437f0000
	v_readlane_b32 s8, v253, 2
	v_readlane_b32 s9, v253, 3
	s_add_u32 s6, s8, 0x4200
	s_addc_u32 s7, s9, 0
	v_readlane_b32 s10, v253, 4
	v_readlane_b32 s11, v253, 5
	v_writelane_b32 v253, s6, 15
	v_mov_b32_e32 v167, 1
	s_mov_b32 s28, 0x800000
	v_writelane_b32 v253, s7, 16
	s_add_u32 s6, s8, 0x4400
	s_addc_u32 s7, s9, 0
	v_writelane_b32 v253, s6, 17
	s_movk_i32 s31, 0x240
	s_mov_b32 s29, 0xf800000
	v_writelane_b32 v253, s7, 18
	s_add_u32 s6, s8, 0x4500
	s_addc_u32 s7, s9, 0
	v_writelane_b32 v253, s6, 19
	v_mov_b32_e32 v214, 0x260
	s_mov_b32 s94, 0xbf1b4598
	v_writelane_b32 v253, s7, 20
	s_add_u32 s6, s8, 0x4600
	s_addc_u32 s7, s9, 0
	v_writelane_b32 v253, s6, 21
	s_movk_i32 s30, 0x7fff
	v_mov_b32_e32 v215, 0xff61b1e6
	v_writelane_b32 v253, s7, 22
	s_add_u32 s6, s8, 0x4700
	s_addc_u32 s7, s9, 0
	v_writelane_b32 v253, s6, 23
	v_mov_b32_e32 v216, 8
	s_mov_b32 s36, 0x42800000
	v_writelane_b32 v253, s7, 24
	s_add_u32 s6, s8, 0x4800
	s_addc_u32 s7, s9, 0
	v_writelane_b32 v253, s6, 25
	v_mov_b32_e32 v217, 0x3a27c5ac
	v_mov_b32_e32 v218, 0x3727c5ac
	v_writelane_b32 v253, s7, 26
	s_add_u32 s6, s8, 0x4900
	s_addc_u32 s7, s9, 0
	v_writelane_b32 v253, s6, 27
	s_mov_b32 s90, 0xc0e00000
	v_mov_b64_e32 v[250:251], 0x6ff
	v_writelane_b32 v253, s7, 28
	s_add_u32 s6, s8, 0x4a00
	s_addc_u32 s7, s9, 0
	v_writelane_b32 v253, s6, 29
	v_mov_b32_e32 v219, 0x41b17218
	v_mov_b32_e32 v252, 0x7ff
	v_writelane_b32 v253, s7, 30
	s_add_u32 s6, s8, 0x4b00
	s_addc_u32 s7, s9, 0
	v_writelane_b32 v253, s6, 31
	v_mov_b32_e32 v224, 0xffffa800
	v_mov_b32_e32 v225, 0x43e00000
	v_writelane_b32 v253, s7, 32
	s_add_u32 s6, s8, 0x4c00
	s_addc_u32 s7, s9, 0
	v_writelane_b32 v253, s6, 33
	v_mov_b32_e32 v166, 0x358637bd
	v_mov_b64_e32 v[168:169], 0x100
	v_writelane_b32 v253, s7, 34
	s_add_u32 s6, s8, 0x4d00
	s_addc_u32 s7, s9, 0
	v_writelane_b32 v253, s6, 35
	v_mov_b64_e32 v[170:171], 0xff
	v_mov_b32_e32 v226, 0x40e00000
	v_writelane_b32 v253, s7, 36
	s_add_u32 s6, s8, 0x4e00
	s_addc_u32 s7, s9, 0
	v_writelane_b32 v253, s6, 37
	s_nop 1
	v_writelane_b32 v253, s7, 38
	s_add_u32 s6, s8, 0x4f00
	s_addc_u32 s7, s9, 0
	v_writelane_b32 v253, s6, 39
	s_nop 1
	v_writelane_b32 v253, s7, 40
	s_add_u32 s6, s8, 0x5000
	s_addc_u32 s7, s9, 0
	v_writelane_b32 v253, s6, 41
	s_nop 1
	v_writelane_b32 v253, s7, 42
	s_add_u32 s6, s8, 0x5100
	s_addc_u32 s7, s9, 0
	v_writelane_b32 v253, s6, 43
	s_nop 1
	v_writelane_b32 v253, s7, 44
	s_add_u32 s6, s8, 0x5200
	s_addc_u32 s7, s9, 0
	v_writelane_b32 v253, s6, 45
	s_nop 1
	v_writelane_b32 v253, s7, 46
	s_add_u32 s6, s8, 0x5300
	s_addc_u32 s7, s9, 0
	v_writelane_b32 v253, s6, 47
	s_cmp_eq_u32 s2, 15
	s_nop 0
	v_writelane_b32 v253, s7, 48
	s_cselect_b64 s[6:7], -1, 0
	v_writelane_b32 v253, s6, 49
	s_cmp_eq_u32 s2, 14
	s_nop 0
	v_writelane_b32 v253, s7, 50
	s_cselect_b64 s[6:7], -1, 0
	v_writelane_b32 v253, s6, 51
	s_cmp_eq_u32 s2, 13
	s_nop 0
	v_writelane_b32 v253, s7, 52
	s_cselect_b64 s[6:7], -1, 0
	v_writelane_b32 v253, s6, 53
	s_cmp_eq_u32 s2, 12
	s_nop 0
	v_writelane_b32 v253, s7, 54
	s_cselect_b64 s[6:7], -1, 0
	v_writelane_b32 v253, s6, 55
	s_cmp_eq_u32 s2, 11
	s_nop 0
	v_writelane_b32 v253, s7, 56
	s_cselect_b64 s[6:7], -1, 0
	v_writelane_b32 v253, s6, 57
	s_cmp_eq_u32 s2, 10
	s_nop 0
	v_writelane_b32 v253, s7, 58
	s_cselect_b64 s[6:7], -1, 0
	v_writelane_b32 v253, s6, 59
	s_cmp_eq_u32 s2, 9
	s_nop 0
	v_writelane_b32 v253, s7, 60
	s_cselect_b64 s[6:7], -1, 0
	v_writelane_b32 v253, s6, 61
	s_cmp_eq_u32 s2, 8
	s_nop 0
	v_writelane_b32 v253, s7, 62
	s_cselect_b64 s[6:7], -1, 0
	v_writelane_b32 v253, s6, 63
	s_cmp_eq_u32 s2, 7
	s_nop 0
	v_writelane_b32 v254, s7, 0
	s_cselect_b64 s[6:7], -1, 0
	v_writelane_b32 v254, s6, 1
	s_cmp_eq_u32 s2, 6
	s_nop 0
	v_writelane_b32 v254, s7, 2
	s_cselect_b64 s[6:7], -1, 0
	v_writelane_b32 v254, s6, 3
	s_cmp_eq_u32 s2, 5
	s_nop 0
	v_writelane_b32 v254, s7, 4
	s_cselect_b64 s[6:7], -1, 0
	v_writelane_b32 v254, s6, 5
	s_cmp_eq_u32 s2, 4
	s_nop 0
	v_writelane_b32 v254, s7, 6
	s_cselect_b64 s[6:7], -1, 0
	v_writelane_b32 v254, s6, 7
	s_cmp_eq_u32 s2, 3
	s_nop 0
	v_writelane_b32 v254, s7, 8
	s_cselect_b64 s[6:7], -1, 0
	v_writelane_b32 v254, s6, 9
	s_cmp_eq_u32 s2, 2
	s_nop 0
	v_writelane_b32 v254, s7, 10
	s_cselect_b64 s[6:7], -1, 0
	v_writelane_b32 v254, s6, 11
	s_cmp_eq_u32 s2, 1
	s_nop 0
	v_writelane_b32 v254, s7, 12
	s_cselect_b64 s[6:7], -1, 0
	v_writelane_b32 v254, s6, 13
	s_cmp_eq_u32 s2, 0
	s_nop 0
	v_writelane_b32 v254, s7, 14
	s_cselect_b64 s[6:7], -1, 0
	s_lshl_b32 s2, s2, 8
	s_add_u32 s0, s0, s2
	v_writelane_b32 v254, s6, 15
	s_addc_u32 s1, s1, 0
	s_mul_i32 s2, s4, 33
	v_writelane_b32 v254, s7, 16
	s_add_u32 s6, s0, 0x1400
	s_addc_u32 s7, s1, 0
	v_writelane_b32 v254, s6, 17
	s_add_u32 s0, s0, 0x2400
	s_addc_u32 s1, s1, 0
	v_writelane_b32 v254, s7, 18
	v_writelane_b32 v254, s0, 19
	v_cmp_eq_u32_e64 s[6:7], 0, v0
	s_nop 0
	v_writelane_b32 v254, s1, 20
	s_add_u32 s0, s8, 0x7400
	s_addc_u32 s1, s9, 0
	v_writelane_b32 v254, s0, 21
	s_nop 1
	v_writelane_b32 v254, s1, 22
	s_add_u32 s0, s8, 0x7500
	s_addc_u32 s1, s9, 0
	v_writelane_b32 v254, s0, 23
	s_cmpk_lt_i32 s92, 0x100
	s_nop 0
	v_writelane_b32 v254, s1, 24
	s_cselect_b64 s[0:1], -1, 0
	v_writelane_b32 v254, s0, 25
	s_nop 1
	v_writelane_b32 v254, s1, 26
	s_lshl_b32 s0, s4, 5
	s_cmp_lt_i32 s4, 0
	s_mul_i32 s1, s4, 0x81
	s_cselect_b32 s1, s1, s5
	s_movk_i32 s5, 0xe1
	s_cselect_b32 s5, s5, 0xe0
	s_cselect_b32 s2, s2, s0
	s_add_i32 s0, s1, s3
	s_ashr_i32 s1, s0, 31
	s_lshr_b32 s1, s1, 25
	v_writelane_b32 v254, s6, 27
	s_add_i32 s1, s0, s1
	s_add_i32 s84, 0, 0x14a00
	v_writelane_b32 v254, s7, 28
	s_ashr_i32 s6, s1, 7
	s_and_b32 s1, s1, 0xff80
	s_sub_i32 s1, s0, s1
	s_bfe_i32 s0, s1, 0x80000
	s_bfe_u32 s0, s0, 0x3000c
	s_add_i32 s7, s1, s0
	s_bfe_i32 s0, s7, 0x80000
	s_and_b32 s7, s7, 0xf8
	s_sub_i32 s1, s1, s7
	s_lshl_b32 s6, s6, 3
	s_sext_i32_i16 s8, s0
	s_sext_i32_i8 s1, s1
	s_add_i32 s10, s6, s1
	s_ashr_i32 s1, s8, 3
	v_writelane_b32 v254, s1, 29
	s_mov_b32 s6, s10
	s_ashr_i32 s11, s10, 31
	v_writelane_b32 v254, s6, 30
	s_lshr_b32 s0, s8, 3
	s_bfe_i64 s[0:1], s[0:1], 0x100000
	v_writelane_b32 v254, s7, 31
	s_lshl_b64 s[6:7], s[10:11], 18
	v_writelane_b32 v254, s6, 32
	s_lshl_b64 s[0:1], s[0:1], 18
	s_add_i32 s85, 0, 0x15200
	v_writelane_b32 v254, s7, 33
	v_writelane_b32 v254, s0, 34
	s_add_i32 s37, 0, 0x15a00
	s_add_i32 s96, 0, 0x16200
	v_writelane_b32 v254, s1, 35
	s_mul_i32 s0, s4, s5
	s_add_i32 s0, s0, s3
	s_mul_hi_i32 s1, s0, 0x92492493
	s_add_i32 s1, s1, s0
	s_lshr_b32 s4, s1, 31
	s_ashr_i32 s1, s1, 7
	s_add_i32 s1, s1, s4
	s_mul_i32 s4, s1, 0xe0
	s_sub_i32 s4, s0, s4
	s_bfe_u32 s0, s4, 0x3001c
	s_add_i32 s5, s4, s0
	s_sext_i32_i16 s6, s5
	s_and_b32 s5, s5, 0xfff8
	s_sub_i32 s4, s4, s5
	s_lshl_b32 s1, s1, 3
	s_sext_i32_i16 s4, s4
	s_add_i32 s8, s1, s4
	s_ashr_i32 s1, s6, 3
	v_writelane_b32 v254, s1, 36
	s_add_i32 s1, s2, s3
	s_ashr_i32 s2, s1, 31
	s_lshr_b32 s2, s2, 27
	s_add_i32 s2, s1, s2
	s_ashr_i32 s3, s2, 5
	s_and_b32 s2, s2, 0xffe0
	s_sub_i32 s1, s1, s2
	s_bfe_i32 s2, s1, 0x80000
	s_bfe_u32 s2, s2, 0x3000c
	s_add_i32 s4, s1, s2
	s_bfe_i32 s2, s4, 0x80000
	s_and_b32 s4, s4, 0xf8
	s_sub_i32 s1, s1, s4
	s_lshl_b32 s3, s3, 3
	s_sext_i32_i8 s1, s1
	s_lshr_b32 s0, s6, 3
	s_sext_i32_i16 s5, s2
	s_add_i32 s6, s3, s1
	s_lshr_b32 s2, s5, 3
	s_ashr_i32 s5, s5, 3
	s_ashr_i32 s7, s6, 31
	v_writelane_b32 v254, s5, 37
	s_lshl_b64 s[4:5], s[6:7], 18
	v_writelane_b32 v254, s4, 38
	s_bfe_i64 s[2:3], s[2:3], 0x100000
	s_ashr_i32 s9, s8, 31
	v_writelane_b32 v254, s5, 39
	s_lshl_b64 s[4:5], s[2:3], 18
	v_writelane_b32 v254, s4, 40
	s_bfe_i64 s[0:1], s[0:1], 0x100000
	s_lshl_b64 s[0:1], s[0:1], 19
	v_writelane_b32 v254, s5, 41
	s_mov_b32 s4, s8
	v_writelane_b32 v254, s4, 42
	s_add_i32 s97, 0, 0x16a00
	s_nop 0
	v_writelane_b32 v254, s5, 43
	s_lshl_b64 s[4:5], s[8:9], 19
	v_writelane_b32 v254, s4, 44
	s_nop 1
	v_writelane_b32 v254, s5, 45
	v_writelane_b32 v254, s0, 46
	s_add_i32 s4, 0, 0x20040
	s_nop 0
	v_writelane_b32 v254, s1, 47
	s_mov_b32 s0, s6
	v_writelane_b32 v254, s0, 48
	s_nop 1
	v_writelane_b32 v254, s1, 49
	s_lshl_b64 s[0:1], s[6:7], 17
	v_writelane_b32 v254, s0, 50
	s_mov_b32 s6, s35
	s_nop 0
	v_writelane_b32 v254, s1, 51
	s_lshl_b64 s[0:1], s[2:3], 17
	v_writelane_b32 v254, s0, 52
	s_add_i32 s2, 0, 0x10400
	s_mov_b32 s3, 0xc3e00000
	v_writelane_b32 v254, s1, 53
	s_mov_b64 s[0:1], 0
	v_writelane_b32 v254, s0, 54
	s_nop 1
	v_writelane_b32 v254, s1, 55
	s_add_i32 s0, 0, 0x11a00
	v_writelane_b32 v254, s0, 56
	s_add_i32 s0, 0, 0x17210
	v_writelane_b32 v254, s0, 57
	s_add_i32 s0, 0, 0x13000
	v_writelane_b32 v254, s0, 58
	s_add_i32 s0, 0, 0x20780
	v_writelane_b32 v254, s0, 59
	v_writelane_b32 v254, s2, 60
	s_add_i32 s2, 0, 0x20640
	v_writelane_b32 v254, s2, 61
	v_writelane_b32 v254, s4, 62
	s_add_i32 s4, 0, 0x20600
	v_writelane_b32 v254, s4, 63
	s_add_i32 s4, 0, 0x20740
	v_writelane_b32 v255, s4, 0
	v_writelane_b32 v255, s83, 1
	v_writelane_b32 v255, s92, 2
	s_movk_i32 s1, 0x5800
	s_mov_b32 s0, 0x3d808081
	s_add_i32 s2, 0, 0x206c0
	v_writelane_b32 v255, s86, 3
	s_branch .LBB0_725

.LBB0_2333:
	s_andn2_b64 vcc, exec, s[6:7]
	s_cbranch_vccnz .LBB0_2404
	v_lshl_add_u32 v8, s82, 6, v0
	s_mov_b32 s6, 0x3fffe0
	v_bfe_i32 v2, v8, 27, 1
	v_lshlrev_b32_e32 v0, 4, v8
	v_lshrrev_b32_e32 v2, 22, v2
	v_add_u32_e32 v2, v0, v2
	v_and_b32_e32 v2, 0xfffffc00, v2
	v_sub_u32_e32 v2, v0, v2
	v_ashrrev_i32_e32 v1, 31, v8
	v_lshrrev_b32_e32 v3, 4, v2
	v_lshrrev_b32_e32 v1, 26, v1
	v_bitop3_b32 v2, v3, v2, 32 bitop3:0x6c
	v_add_u32_e32 v1, v8, v1
	v_ashrrev_i32_e32 v4, 31, v2
	v_ashrrev_i32_e32 v1, 6, v1
	v_lshrrev_b32_e32 v4, 26, v4
	v_lshlrev_b32_e32 v3, 3, v1
	v_add_u32_e32 v4, v2, v4
	v_and_b32_e32 v3, -16, v3
	v_ashrrev_i32_e32 v5, 6, v4
	v_and_b32_e32 v4, 0xc0, v4
	v_add_u32_e32 v3, v5, v3
	v_sub_u32_e32 v2, v2, v4
	v_lshlrev_b32_e32 v1, 5, v1
	v_ashrrev_i16_sdwa v2, v167, sext(v2) dst_sel:DWORD dst_unused:UNUSED_PAD src0_sel:DWORD src1_sel:BYTE_0
	v_lshlrev_b32_e32 v4, 1, v3
	v_lshrrev_b32_e32 v6, 2, v3
	v_and_b32_e32 v5, 3, v5
	v_and_b32_e32 v1, 32, v1
	v_bfe_i32 v2, v2, 0, 16
	v_and_b32_e32 v4, 24, v4
	v_and_b32_e32 v6, 4, v6
	v_and_or_b32 v5, v3, s6, v5
	v_or3_b32 v4, v5, v6, v4
	v_add_lshl_u32 v1, v1, v2, 1
	v_add_u32_e32 v0, 0x2000, v0
	v_lshl_add_u32 v172, v3, 10, v1
	v_lshl_add_u32 v64, v4, 10, v1
	v_ashrrev_i32_e32 v1, 31, v0
	v_lshrrev_b32_e32 v1, 22, v1
	v_add_u32_e32 v1, v0, v1
	v_ashrrev_i32_e32 v1, 10, v1
	v_mul_i32_i24_e32 v2, 0x400, v1
	v_sub_u32_e32 v0, v0, v2
	v_lshrrev_b32_e32 v2, 4, v0
	v_bitop3_b32 v0, v2, v0, 32 bitop3:0x6c
	v_ashrrev_i32_e32 v3, 31, v0
	v_lshrrev_b32_e32 v3, 26, v3
	v_lshlrev_b32_e32 v2, 3, v1
	v_add_u32_e32 v3, v0, v3
	v_and_b32_e32 v2, -16, v2
	v_ashrrev_i32_e32 v4, 6, v3
	v_and_b32_e32 v3, 0xc0, v3
	v_add_u32_e32 v2, v4, v2
	v_sub_u32_e32 v0, v0, v3
	v_lshlrev_b32_e32 v1, 5, v1
	v_ashrrev_i16_sdwa v0, v167, sext(v0) dst_sel:DWORD dst_unused:UNUSED_PAD src0_sel:DWORD src1_sel:BYTE_0
	v_lshlrev_b32_e32 v3, 1, v2
	v_lshrrev_b32_e32 v5, 2, v2
	v_and_b32_e32 v4, 3, v4
	v_and_b32_e32 v1, 32, v1
	v_bfe_i32 v0, v0, 0, 16
	v_and_b32_e32 v3, 24, v3
	v_and_b32_e32 v5, 4, v5
	v_and_or_b32 v4, v2, s6, v4
	v_or3_b32 v3, v4, v5, v3
	v_add_lshl_u32 v0, v1, v0, 1
	v_readfirstlane_b32 s10, v8
	v_mov_b32_e32 v186, 0x7b
	v_mov_b32_e32 v187, 0x79
	v_lshl_add_u32 v174, v2, 10, v0
	v_lshl_add_u32 v176, v3, 10, v0
	s_cmpk_lg_u32 s91, 0x100
	s_cbranch_scc1 .Lpa_keep
	v_readlane_b32 s12, v255, 42
	s_nop 3
	s_cmp_eq_u32 s12, 1
	s_cbranch_scc1 .Lpa_keep
	v_mov_b32_e32 v9, 0x20740
	ds_read_b32 v9, v9
	s_waitcnt lgkmcnt(0)
	v_readfirstlane_b32 s12, v9
	s_nop 3
	s_lshl_b32 s13, s12, 3
	s_and_b32 s13, s13, 0xff
	s_lshl_b32 s14, s12, 2
	s_and_b32 s14, s14, 0xff
	s_cmp_ge_i32 s93, s13
	s_cbranch_scc1 .Lpa_keep
	s_sub_i32 s14, 0x100, s14
	s_cmp_ge_i32 s93, s14
	s_cbranch_scc1 .Lpa_keep
	s_branch .LBB0_2354
.Lpa_keep:
	s_and_b64 vcc, exec, s[38:39]
	s_cbranch_vccnz .LBB0_2354
	s_load_dwordx2 s[8:9], s[4:5], 0x170
	v_readlane_b32 s4, v255, 4
	v_readlane_b32 s5, v255, 5
	s_mov_b32 s5, s35
	v_writelane_b32 v255, s4, 4
	s_waitcnt lgkmcnt(0)
	s_add_u32 s26, s8, 0x8d600000
	s_addc_u32 s27, s9, 0
	v_writelane_b32 v255, s5, 5
	s_lshl_b64 s[4:5], s[4:5], 20
	s_add_u32 s4, s8, s4
	s_addc_u32 s5, s9, s5
	s_add_u32 s33, s4, 0x8f600000
	s_addc_u32 s34, s5, 0
	s_ashr_i32 s11, s10, 6
	s_ashr_i32 s12, s10, 8
	s_lshl_b32 s40, s11, 10
	v_readlane_b32 s4, v254, 40
	v_readlane_b32 s5, v254, 41
	s_add_u32 s22, s33, s4
	s_addc_u32 s23, s34, s5
	s_add_i32 s41, s40, 0
	s_add_i32 m0, s41, 0x10000
	v_mov_b32_e32 v177, v65
	global_load_lds_dwordx4 v64, s[22:23]
	s_add_i32 m0, s41, 0x12000
	s_add_u32 s4, s22, 0x20000
	global_load_lds_dwordx4 v176, s[22:23]
	s_addc_u32 s5, s23, 0
	s_add_i32 m0, s41, 0x14000
	v_mov_b32_e32 v173, v65
	global_load_lds_dwordx4 v64, s[4:5]
	s_add_i32 m0, s41, 0x16000
	v_mov_b32_e32 v175, v65
	global_load_lds_dwordx4 v176, s[4:5]
	v_readlane_b32 s4, v254, 38
	v_readlane_b32 s5, v254, 39
	s_add_u32 s20, s26, s4
	s_addc_u32 s21, s27, s5
	s_add_i32 s42, s41, 0x2000
	s_mov_b32 m0, s41
	s_add_u32 s4, s20, 0x20000
	global_load_lds_dwordx4 v172, s[20:21]
	s_mov_b32 m0, s42
	s_addc_u32 s5, s21, 0
	s_add_i32 s43, s41, 0x4000
	global_load_lds_dwordx4 v174, s[20:21]
	s_mov_b32 m0, s43
	s_add_i32 s44, s41, 0x6000
	global_load_lds_dwordx4 v172, s[4:5]
	s_mov_b32 m0, s44
	s_cmp_eq_u32 s12, 1
	global_load_lds_dwordx4 v174, s[4:5]
	v_lshl_add_u64 v[6:7], s[22:23], 0, v[64:65]
	v_lshl_add_u64 v[4:5], s[22:23], 0, v[176:177]
	v_lshl_add_u64 v[0:1], s[20:21], 0, v[172:173]
	s_cselect_b64 s[4:5], -1, 0
	s_cmp_lg_u32 s12, 1
	v_lshl_add_u64 v[2:3], s[20:21], 0, v[174:175]
	s_cbranch_scc1 .LBB0_2337
	s_barrier

.LBB0_2354:
	v_readlane_b32 s4, v255, 42
	s_nop 3
	s_cmp_eq_u32 s4, 1
	s_cbranch_scc0 .Lpc_norm
	s_mov_b32 s4, 0
	s_nop 0
	v_writelane_b32 v255, s4, 42
	v_readlane_b32 s4, v255, 43
	s_nop 3
	v_writelane_b32 v254, s4, 37
	v_readlane_b32 s4, v255, 44
	s_nop 3
	v_writelane_b32 v254, s4, 38
	v_readlane_b32 s4, v255, 45
	s_nop 3
	v_writelane_b32 v254, s4, 39
	v_readlane_b32 s4, v255, 46
	s_nop 3
	v_writelane_b32 v254, s4, 40
	v_readlane_b32 s4, v255, 47
	s_nop 3
	v_writelane_b32 v254, s4, 41
	v_readlane_b32 s4, v255, 48
	s_nop 3
	v_writelane_b32 v254, s4, 48
	v_readlane_b32 s6, v253, 6
	v_readlane_b32 s7, v253, 7
	s_nop 3
	v_cndmask_b32_e64 v1, 0, 1, s[6:7]
	v_cmp_ne_u32_e64 s[38:39], 1, v1
	v_readlane_b32 s4, v255, 6
	s_nop 3
	s_add_i32 s20, s4, 13
	s_branch .Lpb_back

.LBB0_2432:
	v_readlane_b32 s4, v255, 6
	s_add_i32 s20, s4, 13
	v_readlane_b32 s4, v253, 2
	v_readlane_b32 s7, v253, 5
	s_cmp_ge_i32 s20, s7
	v_readlane_b32 s5, v253, 3
	v_readlane_b32 s6, v253, 4
	s_cbranch_scc1 .LBB0_2482
	s_cmpk_lg_u32 s91, 0x100
	s_cbranch_scc1 .Lpb_done
	v_mov_b32_e32 v0, 0x20740
	ds_read_b32 v0, v0
	s_waitcnt lgkmcnt(0)
	v_readfirstlane_b32 s4, v0
	s_nop 3
	s_lshl_b32 s5, s4, 3
	s_and_b32 s5, s5, 0xff
	s_lshl_b32 s6, s4, 2
	s_and_b32 s6, s6, 0xff
	s_sub_i32 s7, s93, s6
	s_cmp_lt_i32 s7, 0
	s_cbranch_scc1 .Lpb_done
	s_sub_i32 s8, 0x100, s6
	s_min_i32 s8, s8, s5
	s_cmp_ge_i32 s7, s8
	s_cbranch_scc1 .Lpb_done
	s_lshr_b32 s9, s7, 5
	s_lshl_b32 s9, s9, 3
	s_and_b32 s10, s7, 7
	s_add_i32 s12, s9, s10
	s_mov_b32 s13, 0
	s_bfe_u32 s14, s7, 0x20003
	s_mov_b32 s15, 0
	s_mov_b32 s16, s12
	s_mov_b32 s17, s14
	s_lshl_b64 s[12:13], s[12:13], 18
	s_lshl_b64 s[14:15], s[14:15], 18
	v_readlane_b32 s18, v254, 37
	s_nop 3
	v_writelane_b32 v255, s18, 43
	v_readlane_b32 s18, v254, 38
	s_nop 3
	v_writelane_b32 v255, s18, 44
	v_readlane_b32 s18, v254, 39
	s_nop 3
	v_writelane_b32 v255, s18, 45
	v_readlane_b32 s18, v254, 40
	s_nop 3
	v_writelane_b32 v255, s18, 46
	v_readlane_b32 s18, v254, 41
	s_nop 3
	v_writelane_b32 v255, s18, 47
	v_readlane_b32 s18, v254, 48
	s_nop 3
	v_writelane_b32 v255, s18, 48
	v_writelane_b32 v254, s17, 37
	v_writelane_b32 v254, s12, 38
	v_writelane_b32 v254, s13, 39
	v_writelane_b32 v254, s14, 40
	v_writelane_b32 v254, s15, 41
	v_writelane_b32 v254, s16, 48
	s_mov_b32 s18, 1
	s_nop 0
	v_writelane_b32 v255, s18, 42
	v_readlane_b32 s6, v254, 25
	v_readlane_b32 s7, v254, 26
	s_nop 3
	v_cndmask_b32_e64 v1, 0, 1, s[6:7]
	v_cmp_ne_u32_e64 s[38:39], 1, v1
	s_mov_b64 s[4:5], s[80:81]
	s_mov_b64 s[6:7], -1
	v_mbcnt_lo_u32_b32 v0, -1, 0
	v_mbcnt_hi_u32_b32 v0, -1, v0
	s_branch .LBB0_2333
.Lpb_back:
.Lpb_done:
	s_waitcnt vmcnt(0)
	s_barrier
	s_mov_b64 s[4:5], exec
	v_readlane_b32 s6, v254, 27
	v_readlane_b32 s7, v254, 28
	s_and_b64 s[6:7], s[4:5], s[6:7]
	s_mov_b64 exec, s[6:7]
	s_cbranch_execz .LBB0_2481
	v_readlane_b32 s6, v253, 8
	s_waitcnt vmcnt(0) expcnt(0) lgkmcnt(0)
	s_nop 0
	v_mov_b32_e32 v0, s6
	ds_read_b32 v2, v0
	ds_read_b32 v0, v0 offset:4
	s_waitcnt lgkmcnt(1)
	v_cmp_ne_u32_e32 vcc, 0, v2
	s_cbranch_vccnz .LBB0_2449
	v_readlane_b32 s8, v253, 0
	v_readlane_b32 s9, v253, 1
	s_load_dwordx2 s[6:7], s[8:9], 0x4
	s_mov_b32 s13, 1
	s_waitcnt lgkmcnt(0)
	s_mul_i32 s12, s6, s86
	s_mul_i32 s12, s12, s7
	s_branch .LBB0_2437
